# baseline (speedup 1.0000x reference)
.LBB1_6:
	s_waitcnt lgkmcnt(0)
	v_mfma_f32_32x32x16_f16 v[34:49], v[162:165], v[122:125], v[34:49]
	v_exp_f32_e32 v98, v98
	v_exp_f32_e32 v99, v99
	v_exp_f32_e32 v100, v100
	v_exp_f32_e32 v101, v101
	s_sub_i32 s43, s38, s27
	s_add_i32 s43, s43, 34
	s_add_i32 s44, s18, -1
	v_mfma_f32_32x32x16_f16 v[18:33], v[162:165], v[118:121], v[18:33]
	v_exp_f32_e32 v102, v102
	v_exp_f32_e32 v103, v103
	v_exp_f32_e32 v104, v104
	v_exp_f32_e32 v105, v105
	s_cmp_ge_i32 s44, s28
	s_cselect_b32 s45, s28, 0
	s_sub_i32 s44, s44, s45
	v_add_u32_e32 v74, s36, v234
	ds_read_b128 v[62:65], v74
	ds_read_b128 v[138:141], v74 offset:4096
	v_mfma_f32_32x32x16_f16 v[34:49], v[166:169], v[114:117], v[34:49]
	v_exp_f32_e32 v106, v106
	v_exp_f32_e32 v107, v107
	v_exp_f32_e32 v108, v108
	v_exp_f32_e32 v109, v109
	s_and_b64 s[48:49], s[6:7], exec
	s_cselect_b32 s43, s44, s43
	v_mad_i64_i32 v[252:253], s[50:51], s43, v244, v[222:223]
	v_add_u32_e32 v74, s36, v235
	ds_read_b128 v[178:181], v74
	ds_read_b128 v[126:129], v74 offset:4096
	v_mfma_f32_32x32x16_f16 v[18:33], v[166:169], v[70:73], v[18:33]
	v_exp_f32_e32 v110, v110
	v_exp_f32_e32 v111, v111
	v_exp_f32_e32 v112, v112
	v_exp_f32_e32 v113, v113
	s_add_i32 s44, s38, 1
	s_cmp_ge_i32 s44, s29
	s_cselect_b32 s44, s29, 0
	v_add_u32_e32 v70, s36, v236
	ds_read_b128 v[130:133], v70
	ds_read_b128 v[118:121], v70 offset:4096
	v_mfma_f32_32x32x16_f16 v[34:49], v[170:173], v[66:69], v[34:49]
	v_exp_f32_e32 v82, v82
	v_exp_f32_e32 v83, v83
	v_exp_f32_e32 v84, v84
	v_exp_f32_e32 v85, v85
	s_sub_i32 s44, 0, s44
	s_and_b64 s[48:49], s[6:7], exec
	s_cselect_b32 s44, s44, s28
	v_add_u32_e32 v66, s36, v237
	ds_read_b128 v[122:125], v66
	ds_read_b128 v[114:117], v66 offset:4096
	v_mfma_f32_32x32x16_f16 v[18:33], v[170:173], v[50:53], v[18:33]
	v_exp_f32_e32 v86, v86
	v_exp_f32_e32 v87, v87
	v_exp_f32_e32 v88, v88
	v_exp_f32_e32 v89, v89
	s_add_i32 s44, s44, s18
	s_add_i32 s44, s44, -3
	v_mad_i64_i32 v[254:255], s[50:51], s44, v244, v[224:225]
	v_mfma_f32_32x32x16_f16 v[34:49], v[174:177], v[54:57], v[34:49]
	v_exp_f32_e32 v90, v90
	v_exp_f32_e32 v91, v91
	v_exp_f32_e32 v92, v92
	v_exp_f32_e32 v93, v93
	s_add_i32 s52, s35, s30
	s_add_i32 s53, s36, s31
	v_mfma_f32_32x32x16_f16 v[18:33], v[174:177], v[58:61], v[18:33]
	v_exp_f32_e32 v94, v94
	v_exp_f32_e32 v95, v95
	v_exp_f32_e32 v96, v96
	v_exp_f32_e32 v97, v97
	s_mov_b32 m0, s52
	s_addk_i32 s52, 0x1000
	global_load_lds_dwordx4 v[252:253], off
	s_mov_b32 m0, s52
	v_lshl_add_u64 v[252:253], v[252:253], 0, s[10:11]
	global_load_lds_dwordx4 v[252:253], off
	s_mov_b32 m0, s53
	s_addk_i32 s53, 0x1000
	global_load_lds_dwordx4 v[254:255], off
	s_mov_b32 m0, s53
	v_lshl_add_u64 v[254:255], v[254:255], 0, s[10:11]
	global_load_lds_dwordx4 v[254:255], off
	s_waitcnt vmcnt(4) lgkmcnt(0)
	s_barrier
	s_andn2_b64 vcc, exec, s[8:9]
	s_cbranch_vccnz .LBB1_12
	v_add_u32_e32 v66, s24, v233
	ds_read_b128 v[50:53], v66 offset:96
	ds_read_b128 v[54:57], v66 offset:64
	ds_read_b128 v[58:61], v66 offset:32
	ds_read_b128 v[66:69], v66
	s_waitcnt lgkmcnt(3)
	v_pk_mul_f32 v[46:47], v[46:47], v[50:51]
	s_waitcnt lgkmcnt(2)
	v_pk_mul_f32 v[42:43], v[42:43], v[54:55]
	s_waitcnt lgkmcnt(1)
	v_pk_mul_f32 v[38:39], v[38:39], v[58:59]
	v_pk_mul_f32 v[48:49], v[48:49], v[52:53]
	v_pk_mul_f32 v[44:45], v[44:45], v[56:57]
	v_pk_mul_f32 v[40:41], v[40:41], v[60:61]
	s_waitcnt lgkmcnt(0)
	v_pk_mul_f32 v[36:37], v[36:37], v[68:69]
	v_pk_mul_f32 v[34:35], v[34:35], v[66:67]
	v_pk_mul_f32 v[30:31], v[30:31], v[50:51]
	v_pk_mul_f32 v[26:27], v[26:27], v[54:55]
	v_pk_mul_f32 v[22:23], v[22:23], v[58:59]
	v_pk_mul_f32 v[32:33], v[32:33], v[52:53]
	v_pk_mul_f32 v[28:29], v[28:29], v[56:57]
	v_pk_mul_f32 v[24:25], v[24:25], v[60:61]
	v_pk_mul_f32 v[20:21], v[20:21], v[68:69]
	v_pk_mul_f32 v[18:19], v[18:19], v[66:67]

.LBB1_13:
	s_add_i32 s16, s36, 0x2000
	s_cmpk_lg_i32 s36, 0x4000
	s_cselect_b32 s35, s16, 0
	s_waitcnt lgkmcnt(0)
	v_mfma_f32_32x32x16_f16 v[34:49], v[162:165], v[134:137], v[34:49]
	v_exp_f32_e32 v66, v66
	v_exp_f32_e32 v67, v67
	v_exp_f32_e32 v68, v68
	v_exp_f32_e32 v69, v69
	s_sub_i32 s43, s38, s27
	s_add_i32 s45, s43, 33
	s_add_i32 s43, s43, 35
	v_mfma_f32_32x32x16_f16 v[18:33], v[162:165], v[142:145], v[18:33]
	v_exp_f32_e32 v70, v70
	v_exp_f32_e32 v71, v71
	v_exp_f32_e32 v72, v72
	v_exp_f32_e32 v73, v73
	s_cmp_ge_i32 s18, s28
	s_cselect_b32 s44, s28, 0
	s_sub_i32 s44, s18, s44
	v_add_u32_e32 v94, s35, v234
	ds_read_b128 v[206:209], v94
	ds_read_b128 v[202:205], v94 offset:4096
	v_mfma_f32_32x32x16_f16 v[34:49], v[166:169], v[138:141], v[34:49]
	v_exp_f32_e32 v74, v74
	v_exp_f32_e32 v75, v75
	v_exp_f32_e32 v76, v76
	v_exp_f32_e32 v77, v77
	s_and_b64 s[48:49], s[6:7], exec
	s_cselect_b32 s43, s44, s43
	v_mad_i64_i32 v[252:253], s[50:51], s43, v244, v[222:223]
	v_add_u32_e32 v94, s35, v235
	ds_read_b128 v[198:201], v94
	ds_read_b128 v[194:197], v94 offset:4096
	v_mfma_f32_32x32x16_f16 v[18:33], v[166:169], v[102:105], v[18:33]
	v_exp_f32_e32 v78, v78
	v_exp_f32_e32 v79, v79
	v_exp_f32_e32 v80, v80
	v_exp_f32_e32 v81, v81
	s_add_i32 s44, s18, -2
	s_cmp_ge_i32 s44, s28
	s_cselect_b32 s46, s28, 0
	v_add_u32_e32 v94, s35, v236
	ds_read_b128 v[190:193], v94
	ds_read_b128 v[186:189], v94 offset:4096
	v_mfma_f32_32x32x16_f16 v[34:49], v[170:173], v[98:101], v[34:49]
	v_exp_f32_e32 v50, v50
	v_exp_f32_e32 v51, v51
	v_exp_f32_e32 v52, v52
	v_exp_f32_e32 v53, v53
	s_sub_i32 s44, s44, s46
	s_and_b64 s[48:49], s[6:7], exec
	s_cselect_b32 s44, s44, s45
	v_add_u32_e32 v94, s35, v237
	ds_read_b128 v[182:185], v94
	ds_read_b128 v[178:181], v94 offset:4096
	v_mfma_f32_32x32x16_f16 v[18:33], v[170:173], v[82:85], v[18:33]
	v_exp_f32_e32 v54, v54
	v_exp_f32_e32 v55, v55
	v_exp_f32_e32 v56, v56
	v_exp_f32_e32 v57, v57
	v_mad_i64_i32 v[254:255], s[50:51], s44, v244, v[224:225]
	s_add_i32 s52, s36, s30
	s_add_i32 s53, s35, s31
	v_mfma_f32_32x32x16_f16 v[34:49], v[174:177], v[86:89], v[34:49]
	v_exp_f32_e32 v58, v58
	v_exp_f32_e32 v59, v59
	v_exp_f32_e32 v60, v60
	v_exp_f32_e32 v61, v61
	s_add_i32 s46, s35, 0x2000
	s_cmpk_lg_i32 s35, 0x4000
	s_cselect_b32 s37, s46, 0
	v_mfma_f32_32x32x16_f16 v[18:33], v[174:177], v[90:93], v[18:33]
	v_exp_f32_e32 v62, v62
	v_exp_f32_e32 v63, v63
	v_exp_f32_e32 v64, v64
	v_exp_f32_e32 v65, v65
	s_add_i32 s39, s18, -2
	s_mov_b32 m0, s52
	s_addk_i32 s52, 0x1000
	global_load_lds_dwordx4 v[252:253], off
	s_mov_b32 m0, s52
	v_lshl_add_u64 v[252:253], v[252:253], 0, s[10:11]
	global_load_lds_dwordx4 v[252:253], off
	s_mov_b32 m0, s53
	s_addk_i32 s53, 0x1000
	global_load_lds_dwordx4 v[254:255], off
	s_mov_b32 m0, s53
	v_lshl_add_u64 v[254:255], v[254:255], 0, s[10:11]
	global_load_lds_dwordx4 v[254:255], off
	s_waitcnt vmcnt(4) lgkmcnt(0)
	s_barrier
	s_andn2_b64 vcc, exec, s[8:9]
	s_cbranch_vccnz .LBB1_23
	v_add_u32_e32 v94, s24, v233
	ds_read_b128 v[82:85], v94 offset:96
	ds_read_b128 v[86:89], v94 offset:64
	ds_read_b128 v[90:93], v94
	ds_read_b128 v[94:97], v94 offset:32
	s_waitcnt lgkmcnt(3)
	v_pk_mul_f32 v[48:49], v[48:49], v[84:85]
	v_pk_mul_f32 v[46:47], v[46:47], v[82:83]
	s_waitcnt lgkmcnt(2)
	v_pk_mul_f32 v[44:45], v[44:45], v[88:89]
	v_pk_mul_f32 v[42:43], v[42:43], v[86:87]
	s_waitcnt lgkmcnt(0)
	v_pk_mul_f32 v[40:41], v[40:41], v[96:97]
	v_pk_mul_f32 v[38:39], v[38:39], v[94:95]
	v_pk_mul_f32 v[36:37], v[36:37], v[92:93]
	v_pk_mul_f32 v[34:35], v[34:35], v[90:91]
	v_pk_mul_f32 v[32:33], v[32:33], v[84:85]
	v_pk_mul_f32 v[30:31], v[30:31], v[82:83]
	v_pk_mul_f32 v[28:29], v[28:29], v[88:89]
	v_pk_mul_f32 v[26:27], v[26:27], v[86:87]
	v_pk_mul_f32 v[24:25], v[24:25], v[96:97]
	v_pk_mul_f32 v[22:23], v[22:23], v[94:95]
	v_pk_mul_f32 v[20:21], v[20:21], v[92:93]
	v_pk_mul_f32 v[18:19], v[18:19], v[90:91]
